# DA loop cleanup: second score block takes the running-max vector as SrcC (8 v_mov_b64 gone), dead prefetch compare/branch at the tile barrier removed; m1
# baseline (speedup 1.0000x reference)
; __device__ __forceinline__ void da_unit(LAS unsigned char* lds, const bf16* __restrict__ Q, const bf16* __restrict__ Kp, const bf16* __restrict__ Vp, const float* __restrict__ gda, float lam, ...
;     ...
;     for (int j = 0; j < NT; ++j) {
;         const int buf = kbuf;
;         if (j + 1 < NT) asm volatile("s_waitcnt vmcnt(4)" ::: "memory"); else asm volatile("s_waitcnt vmcnt(0)" ::: "memory");
;         __syncthreads();
;         if (j + 2 < NT) att_dma(dm, Kh, Vh, (j + 2) * 64, K_lds + (kbuf == 0 ? 2 : kbuf - 1) * SHM_T, V_lds + ((vbuf + 2) & 3) * SHM_T, wave);
;         if (comp == 1 && pend) { pv_pipe(o, vb0 + pbuf * SHM_T, pa0, pa1, pa2, pa3); pend = false; }
.LBB0_579:
	s_barrier
	s_and_b64 s[8:9], s[12:13], s[18:19]
	s_andn2_b64 vcc, exec, s[8:9]
	s_cbranch_vccz .LBB0_583

; #define LAS __attribute__((address_space(3)))
; #define SBAR() __builtin_amdgcn_sched_barrier(0)
; __device__ __forceinline__ void da_unit(LAS unsigned char* lds, const bf16* __restrict__ Q, const bf16* __restrict__ Kp, const bf16* __restrict__ Vp, const float* __restrict__ gda, float lam, ...
;     ...
;         if (j + 2 < NT) att_dma(dm, Kh, Vh, (j + 2) * 64, K_lds + (kbuf == 0 ? 2 : kbuf - 1) * SHM_T, V_lds + ((vbuf + 2) & 3) * SHM_T, wave);
;         if (comp == 1 && pend) { pv_pipe(o, vb0 + pbuf * SHM_T, pa0, pa1, pa2, pa3); pend = false; }
;         if (j < NTw) {
;             f32x16 p0 = mneg, p1 = mneg;
;             { const LAS unsigned char* Ks = K_lds + buf * SHM_T; bf16x8 kb0[4], kb1[4];
; #pragma unroll
;               for (int d0 = 0; d0 < 4; ++d0) { const int cb = (comp * 64 + d0 * 16 + hi * 8) * 2;
;                   kb0[d0] = *(const LAS bf16x8*)(Ks + KSWZ(r32, cb)); kb1[d0] = *(const LAS bf16x8*)(Ks + KSWZ(32 + r32, cb)); }
;               SBAR();
; #pragma unroll
;               for (int d0 = 0; d0 < 4; ++d0) { p0 = __builtin_amdgcn_mfma_f32_32x32x16_bf16(kb0[d0], qr[d0], p0, 0, 0, 0); p1 = __builtin_amdgcn_mfma_f32_32x32x16_bf16(kb1[d0], qr[d0], p1, 0, 0, 0); } }
.LBB0_584:
	s_lshl_b32 s8, s23, 14
	s_add_i32 s8, s8, 0
	s_add_i32 s8, s8, 0x10000
	v_add_u32_e32 v82, s8, v165
	v_add_u32_e32 v83, s8, v170
	v_add_u32_e32 v84, v82, v173
	v_add_u32_e32 v85, v83, v173
	ds_read_b128 v[98:101], v84
	ds_read_b128 v[182:185], v85
	v_add_u32_e32 v84, v82, v174
	v_add_u32_e32 v85, v83, v174
	ds_read_b128 v[186:189], v84
	ds_read_b128 v[190:193], v85
	v_add_u32_e32 v84, v82, v175
	v_add_u32_e32 v82, v82, v176
	v_add_u32_e32 v85, v83, v175
	ds_read_b128 v[196:199], v84
	ds_read_b128 v[200:203], v85
	v_add_u32_e32 v83, v83, v176
	ds_read_b128 v[204:207], v82
	ds_read_b128 v[208:211], v83
	s_waitcnt lgkmcnt(7)
	s_setprio 1
	v_mfma_f32_32x32x16_bf16 v[82:97], v[98:101], v[114:117], v[66:81]
	s_waitcnt lgkmcnt(5)
	v_mfma_f32_32x32x16_bf16 v[82:97], v[186:189], v[118:121], v[82:97]
	s_mov_b32 s8, 0x4138aa3b
	v_mfma_f32_32x32x16_bf16 v[98:113], v[182:185], v[114:117], v[66:81]
	s_waitcnt lgkmcnt(3)
	v_mfma_f32_32x32x16_bf16 v[82:97], v[196:199], v[122:125], v[82:97]
	v_mfma_f32_32x32x16_bf16 v[98:113], v[190:193], v[118:121], v[98:113]
	s_waitcnt lgkmcnt(1)
	v_mfma_f32_32x32x16_bf16 v[82:97], v[204:207], v[126:129], v[82:97]
	v_mfma_f32_32x32x16_bf16 v[98:113], v[200:203], v[122:125], v[98:113]
	s_add_i32 s98, s27, 5
	s_cmp_ge_u32 s98, s24
	s_cbranch_scc1 .Lda_nodma
	s_lshl_b32 s98, s23, 14
	s_addk_i32 s98, 0xc000
	s_cmp_lg_u32 s23, 0
	s_cselect_b32 s98, s98, 0x8000
	s_lshl_b32 s99, s29, 14
	s_xor_b32 s99, s99, 0x8000
	s_add_i32 s98, s76, s98
	s_mov_b32 m0, s98
	s_add_i32 s99, s57, s99
	buffer_load_dwordx4 v247, s[4:7], s28 offen lds
	s_mov_b32 s66, s6
	s_mov_b32 s67, s7
	s_mov_b32 m0, s99
	s_nop 0
	buffer_load_dwordx4 v137, s[64:67], s28 offen lds
	s_add_i32 m0, s98, 0x2000
	s_nop 0
	buffer_load_dwordx4 v248, s[4:7], s28 offen lds
	s_add_i32 m0, s99, 0x2000
	s_nop 0
	buffer_load_dwordx4 v141, s[64:67], s28 offen lds
	s_branch .Lda_dmadone
